# v55 + static s_setprio 1 for waves 4-7 at the unit-loop head of the attention phases (FoX, DSA attention, diff attention, MLA)
# speedup vs baseline: 1.0073x; 1.0073x over previous
; template <int PH>
; __device__ __forceinline__ void mk_body(const Args& a) {
;     ...
;         for (;;) {
;             const int u = att::next_unit_pre(qp, ctl + CW_Q + 0 * 512, 256, lds, att::OFF_MISC, wave);
;             if (u < 0) break;
;             const int b = u >> 8, h = 2 * ((u >> 6) & 3) + ((u >> 4) & 1), qb = ((u >> 5) & 1) ? 15 - (u & 15) : 31 - (u & 15);
.LBB0_616:
	v_readlane_b32 s100, v254, 24
	s_cmp_lt_u32 s100, 4
	s_cbranch_scc1 .Lprio_0
	s_setprio 1
